# v31
# speedup vs baseline: 1.0106x; 1.0106x over previous
.LBB0_15:
	s_andn2_b64 vcc, exec, s[24:25]
	s_cbranch_vccnz .LBB0_17
	s_lshl_b32 s24, s26, 14
	s_add_i32 s24, s24, s33
	s_or_b32 s25, s24, 0x1000
	buffer_load_dwordx4 v[34:37], v204, s[12:15], s24 offen sc0 nt sc1
	buffer_load_dwordx4 v[38:41], v204, s[12:15], s25 offen sc0 nt sc1
	s_nop 3
	s_or_b32 s25, s24, 0x2000
	s_or_b32 s27, s24, 0x3000
	buffer_load_dwordx4 v[42:45], v204, s[12:15], s25 offen sc0 nt sc1
	buffer_load_dwordx4 v[46:49], v204, s[12:15], s27 offen sc0 nt sc1
	s_nop 3
	s_or_b32 s25, s24, 0x400
	s_or_b32 s27, s24, 0x1400
	buffer_load_dwordx4 v[50:53], v204, s[12:15], s25 offen sc0 nt sc1
	buffer_load_dwordx4 v[54:57], v204, s[12:15], s27 offen sc0 nt sc1
	s_nop 3
	s_or_b32 s25, s24, 0x2400
	s_or_b32 s27, s24, 0x3400
	buffer_load_dwordx4 v[58:61], v204, s[12:15], s25 offen sc0 nt sc1
	buffer_load_dwordx4 v[62:65], v204, s[12:15], s27 offen sc0 nt sc1
	s_nop 3
	s_or_b32 s25, s24, 0x800
	s_or_b32 s27, s24, 0x1800
	buffer_load_dwordx4 v[66:69], v204, s[12:15], s25 offen sc0 nt sc1
	buffer_load_dwordx4 v[70:73], v204, s[12:15], s27 offen sc0 nt sc1
	s_nop 3
	s_or_b32 s25, s24, 0x2800
	s_or_b32 s27, s24, 0x3800
	buffer_load_dwordx4 v[74:77], v204, s[12:15], s25 offen sc0 nt sc1
	buffer_load_dwordx4 v[78:81], v204, s[12:15], s27 offen sc0 nt sc1
	s_nop 3
	s_or_b32 s25, s24, 0xc00
	s_or_b32 s27, s24, 0x1c00
	buffer_load_dwordx4 v[82:85], v204, s[12:15], s25 offen sc0 nt sc1
	buffer_load_dwordx4 v[86:89], v204, s[12:15], s27 offen sc0 nt sc1
	s_nop 3
	s_or_b32 s25, s24, 0x2c00
	s_or_b32 s24, s24, 0x3c00
	buffer_load_dwordx4 v[90:93], v204, s[12:15], s25 offen sc0 nt sc1
	buffer_load_dwordx4 v[94:97], v204, s[12:15], s24 offen sc0 nt sc1
